# baseline (speedup 1.0000x reference)
.LBB0_60:
	s_andn2_b64 vcc, exec, s[4:5]
	s_cbranch_vccnz .LBB0_98
	s_cmpk_gt_u32 s2, 244
	s_cbranch_scc1 .LBB0_98
	s_load_dwordx2 s[4:5], s[0:1], 0x0
	s_load_dwordx4 s[12:15], s[0:1], 0x30
	s_lshl_b32 s3, s2, 12
	v_lshlrev_b32_e32 v1, 2, v0
	v_mov_b32_e32 v2, 0
	ds_write_b32 v1, v2
	v_or_b32_e32 v3, s3, v0
	s_mov_b32 s10, 0xf423f
	s_waitcnt lgkmcnt(0)
	s_add_u32 s6, s4, 0x3d0900
	s_addc_u32 s7, s5, 0
	v_min_u32_e32 v4, s10, v3
	v_lshlrev_b32_e32 v4, 2, v4
	global_load_dword v16, v4, s[6:7] nt
	global_load_dword v32, v4, s[4:5] nt
	v_add_u32_e32 v5, 1024, v3
	v_min_u32_e32 v5, s10, v5
	v_lshlrev_b32_e32 v5, 2, v5
	global_load_dword v17, v5, s[6:7] nt
	global_load_dword v33, v5, s[4:5] nt
	v_add_u32_e32 v6, 2048, v3
	v_min_u32_e32 v6, s10, v6
	v_lshlrev_b32_e32 v6, 2, v6
	global_load_dword v18, v6, s[6:7] nt
	global_load_dword v34, v6, s[4:5] nt
	v_add_u32_e32 v7, 3072, v3
	v_min_u32_e32 v7, s10, v7
	v_lshlrev_b32_e32 v7, 2, v7
	global_load_dword v19, v7, s[6:7] nt
	global_load_dword v35, v7, s[4:5] nt
	s_barrier
	s_mov_b32 s11, 0x5397829d
	s_mov_b32 s10, 0xf4240
	v_mov_b32_e32 v8, 0xffc
	s_waitcnt vmcnt(0)
	v_cmp_gt_u32_e32 vcc, s10, v3
	v_mul_hi_u32 v4, v16, s11
	v_lshrrev_b32_e32 v4, 5, v4
	v_mul_u32_u24_e32 v5, 0x62, v4
	v_sub_u32_e32 v5, v16, v5
	v_lshl_or_b32 v32, v5, 17, v32
	v_lshlrev_b32_e32 v4, 2, v4
	v_cndmask_b32_e32 v16, v8, v4, vcc
	v_add_u32_e32 v6, 1024, v3
	v_cmp_gt_u32_e32 vcc, s10, v6
	v_mul_hi_u32 v4, v17, s11
	v_lshrrev_b32_e32 v4, 5, v4
	v_mul_u32_u24_e32 v5, 0x62, v4
	v_sub_u32_e32 v5, v17, v5
	v_lshl_or_b32 v33, v5, 17, v33
	v_lshlrev_b32_e32 v4, 2, v4
	v_cndmask_b32_e32 v17, v8, v4, vcc
	v_add_u32_e32 v6, 2048, v3
	v_cmp_gt_u32_e32 vcc, s10, v6
	v_mul_hi_u32 v4, v18, s11
	v_lshrrev_b32_e32 v4, 5, v4
	v_mul_u32_u24_e32 v5, 0x62, v4
	v_sub_u32_e32 v5, v18, v5
	v_lshl_or_b32 v34, v5, 17, v34
	v_lshlrev_b32_e32 v4, 2, v4
	v_cndmask_b32_e32 v18, v8, v4, vcc
	v_add_u32_e32 v6, 3072, v3
	v_cmp_gt_u32_e32 vcc, s10, v6
	v_mul_hi_u32 v4, v19, s11
	v_lshrrev_b32_e32 v4, 5, v4
	v_mul_u32_u24_e32 v5, 0x62, v4
	v_sub_u32_e32 v5, v19, v5
	v_lshl_or_b32 v35, v5, 17, v35
	v_lshlrev_b32_e32 v4, 2, v4
	v_cndmask_b32_e32 v19, v8, v4, vcc
	v_mov_b32_e32 v7, 1
	ds_add_rtn_u32 v48, v16, v7
	ds_add_rtn_u32 v49, v17, v7
	ds_add_rtn_u32 v50, v18, v7
	ds_add_rtn_u32 v51, v19, v7
	s_waitcnt lgkmcnt(0)
	s_barrier
	ds_read_b32 v4, v1
	v_and_b32_e32 v8, 63, v0
	v_lshrrev_b32_e32 v9, 6, v0
	s_waitcnt lgkmcnt(0)
	v_add_u32_dpp v5, v4, v4 row_shr:1 row_mask:0xf bank_mask:0xf bound_ctrl:1
	s_nop 1
	v_add_u32_dpp v5, v5, v5 row_shr:2 row_mask:0xf bank_mask:0xf bound_ctrl:1
	s_nop 1
	v_add_u32_dpp v5, v5, v5 row_shr:4 row_mask:0xf bank_mask:0xf bound_ctrl:1
	s_nop 1
	v_add_u32_dpp v5, v5, v5 row_shr:8 row_mask:0xf bank_mask:0xf bound_ctrl:1
	s_nop 1
	v_add_u32_dpp v5, v5, v5 row_bcast:15 row_mask:0xa bank_mask:0xf
	s_nop 1
	v_add_u32_dpp v5, v5, v5 row_bcast:31 row_mask:0xc bank_mask:0xf
	v_readfirstlane_b32 s9, v9
	s_nop 0
	v_readlane_b32 s8, v5, 63
	s_lshl_b32 s16, s9, 2
	v_mov_b32_e32 v10, s16
	s_nop 1
	v_mov_b32_e32 v11, s8
	ds_write_b32 v10, v11 offset:4096
	s_waitcnt lgkmcnt(0)
	s_barrier
	v_min_u32_e32 v10, 15, v8
	v_lshlrev_b32_e32 v10, 2, v10
	ds_read_b32 v11, v10 offset:4096
	v_cmp_gt_u32_e32 vcc, s9, v8
	v_sub_u32_e32 v5, v5, v4
	s_waitcnt lgkmcnt(0)
	v_cndmask_b32_e32 v11, 0, v11, vcc
	s_nop 1
	v_add_u32_dpp v11, v11, v11 row_shr:1 row_mask:0xf bank_mask:0xf bound_ctrl:1
	s_nop 1
	v_add_u32_dpp v11, v11, v11 row_shr:2 row_mask:0xf bank_mask:0xf bound_ctrl:1
	s_nop 1
	v_add_u32_dpp v11, v11, v11 row_shr:4 row_mask:0xf bank_mask:0xf bound_ctrl:1
	s_nop 1
	v_add_u32_dpp v11, v11, v11 row_shr:8 row_mask:0xf bank_mask:0xf bound_ctrl:1
	s_nop 1
	v_readlane_b32 s17, v11, 15
	s_nop 3
	v_add_u32_e32 v5, s17, v5
	ds_write_b32 v1, v5
	s_waitcnt lgkmcnt(0)
	s_barrier
	s_sleep 127
	s_mulk_i32 s2, 0x3fe
	v_add_u32_e32 v10, s2, v0
	v_lshlrev_b32_e32 v10, 2, v10
	s_movk_i32 s16, 0x3fe
	v_cmp_gt_u32_e32 vcc, s16, v0
	s_and_saveexec_b64 s[8:9], vcc
	s_cbranch_execz .Lk1p_o
	global_store_dword v10, v5, s[14:15] sc1
